# P8 routing tables: one returning atomic per expert per workgroup (wave totals through LDS, per-wave prefix) instead of one per wave
# speedup vs baseline: 1.0194x; 1.0123x over previous
.LBB0_764:
	s_ashr_i32 s41, s40, 31
	s_lshr_b32 s22, s41, 17
	s_add_i32 s2, s40, s22
	s_ashr_i32 s23, s2, 15
	v_bcnt_u32_b32 v4, v6, 0
	s_lshl_b32 s98, s76, 8
	s_add_i32 s98, s98, 0x21800
	v_lshl_add_u32 v20, v100, 2, s98
	ds_write_b32 v20, v4
	s_waitcnt lgkmcnt(0)
	s_barrier
	v_lshlrev_b32_e32 v21, 2, v100
	v_add_u32_e32 v21, 0x21800, v21
	ds_read_b32 v22, v21
	ds_read_b32 v23, v21 offset:256
	ds_read_b32 v24, v21 offset:512
	ds_read_b32 v25, v21 offset:768
	ds_read_b32 v26, v21 offset:1024
	ds_read_b32 v27, v21 offset:1280
	ds_read_b32 v28, v21 offset:1536
	ds_read_b32 v29, v21 offset:1792
	v_mov_b32_e32 v30, 0
	s_waitcnt lgkmcnt(0)
	s_cmp_gt_u32 s76, 0
	s_cselect_b32 s99, -1, 0
	v_and_b32_e32 v31, s99, v22
	v_add_u32_e32 v30, v30, v31
	s_cmp_gt_u32 s76, 1
	s_cselect_b32 s99, -1, 0
	v_and_b32_e32 v31, s99, v23
	v_add_u32_e32 v30, v30, v31
	s_cmp_gt_u32 s76, 2
	s_cselect_b32 s99, -1, 0
	v_and_b32_e32 v31, s99, v24
	v_add_u32_e32 v30, v30, v31
	s_cmp_gt_u32 s76, 3
	s_cselect_b32 s99, -1, 0
	v_and_b32_e32 v31, s99, v25
	v_add_u32_e32 v30, v30, v31
	s_cmp_gt_u32 s76, 4
	s_cselect_b32 s99, -1, 0
	v_and_b32_e32 v31, s99, v26
	v_add_u32_e32 v30, v30, v31
	s_cmp_gt_u32 s76, 5
	s_cselect_b32 s99, -1, 0
	v_and_b32_e32 v31, s99, v27
	v_add_u32_e32 v30, v30, v31
	s_cmp_gt_u32 s76, 6
	s_cselect_b32 s99, -1, 0
	v_and_b32_e32 v31, s99, v28
	v_add_u32_e32 v30, v30, v31
	s_cmp_gt_u32 s76, 7
	s_cselect_b32 s99, -1, 0
	v_and_b32_e32 v31, s99, v29
	v_add_u32_e32 v30, v30, v31
	v_add3_u32 v32, v22, v23, v24
	v_add3_u32 v32, v32, v25, v26
	v_add3_u32 v32, v32, v27, v28
	v_add_u32_e32 v32, v32, v29
	v_mov_b32_e32 v2, 0
	s_cmp_lg_u32 s76, 0
	s_cbranch_scc1 .Lp8a_w
	v_cmp_ne_u32_e32 vcc, 0, v32
	s_and_saveexec_b64 s[2:3], vcc
	s_cbranch_execz .Lp8a_n
	v_lshl_or_b32 v2, s23, 6, v100
	v_ashrrev_i32_e32 v3, 31, v2
	v_lshl_add_u64 v[2:3], v[2:3], 2, s[34:35]
	global_atomic_add v2, v[2:3], v32, off sc0
.Lp8a_n:
	s_or_b64 exec, exec, s[2:3]
	v_add_u32_e32 v33, 0x800, v21
	s_waitcnt vmcnt(0)
	ds_write_b32 v33, v2
	s_waitcnt lgkmcnt(0)
.Lp8a_w:
	s_barrier
	v_add_u32_e32 v33, 0x800, v21
	ds_read_b32 v2, v33
	s_waitcnt lgkmcnt(0)
	v_add_u32_e32 v2, v2, v30
	s_mul_i32 s2, s23, 0x41
	s_ashr_i32 s3, s2, 31
	v_lshl_add_u64 v[4:5], s[2:3], 0, v[100:101]
	v_and_b32_e32 v8, 1, v7
	v_lshlrev_b64 v[4:5], 15, v[4:5]
	v_cmp_eq_u32_e64 s[2:3], 1, v8
	v_cmp_ne_u32_e32 vcc, 0, v8
	s_and_saveexec_b64 s[20:21], s[2:3]
	s_cbranch_execz .LBB0_768
	v_and_b32_e32 v9, vcc_lo, v122
	v_and_b32_e32 v3, vcc_hi, v1
	v_bcnt_u32_b32 v9, v9, 0
	v_bcnt_u32_b32 v10, v3, v9
	s_waitcnt vmcnt(0)
	v_ashrrev_i32_e32 v3, 31, v2
	s_lshl_b32 s2, s23, 15
	v_lshl_add_u64 v[12:13], v[4:5], 0, v[2:3]
	s_sub_i32 s2, s40, s2
	v_lshlrev_b64 v[12:13], 2, v[12:13]
	v_lshl_add_u64 v[14:15], s[24:25], 0, v[12:13]
	v_mov_b32_e32 v3, s2
	global_store_dword v[14:15], v3, off
	v_mov_b32_e32 v3, s45
	ds_read_b32 v9, v180
	ds_read_b32 v3, v3 offset:256
	v_mad_u64_u32 v[14:15], s[2:3], s2, 9, v[10:11]
	s_lshl_b64 s[2:3], s[40:41], 5
	s_add_u32 s2, s43, s2
	v_lshl_add_u64 v[12:13], s[26:27], 0, v[12:13]
	s_waitcnt lgkmcnt(0)
	v_mul_f32_e32 v3, v9, v3
	s_addc_u32 s3, s44, s3
	v_lshlrev_b32_e32 v9, 2, v10
	global_store_dword v[12:13], v14, off
	global_store_dword v9, v3, s[2:3]
